# v86 + block-prologue de-serialisation: the K(1..3)/ck(1..3) and V(1) LDS-DMA of each attention block issued inside the block prologue right behind its tile-0 DMAs (one wait covers both) instead of aft
# baseline (speedup 1.0000x reference)
.LBB0_1086:
	v_mbcnt_lo_u32_b32 v146, -1, 0
	v_mbcnt_hi_u32_b32 v146, -1, v146
	s_and_b64 s[2:3], s[4:5], exec
	v_ashrrev_i32_e32 v4, 5, v146
	v_ashrrev_i32_e32 v11, 4, v146
	v_and_b32_e32 v13, 15, v146
	v_lshrrev_b32_e32 v0, 1, v146
	v_mov_b32_e32 v7, s56
	v_lshlrev_b32_e32 v7, 1, v7
	v_and_b32_e32 v7, 8, v7
	v_or_b32_e32 v7, v7, v11
	v_xor_b32_e32 v7, v7, v13
	v_add_u32_e32 v8, s56, v4
	v_bfe_u32 v2, v146, 2, 2
	v_and_b32_e32 v5, 8, v0
	v_lshlrev_b32_e32 v10, 4, v7
	v_lshlrev_b32_e32 v7, 1, v8
	v_or_b32_e32 v14, v5, v2
	v_and_b32_e32 v7, -16, v7
	v_and_b32_e32 v8, 4, v8
	v_lshlrev_b32_e32 v12, 4, v146
	v_or3_b32 v15, v8, v7, v14
	v_lshlrev_b32_e32 v9, 6, v4
	v_and_b32_e32 v3, 48, v12
	v_and_b32_e32 v9, 0xc0, v9
	v_lshlrev_b32_e32 v15, 12, v15
	v_or3_b32 v19, v15, v9, v3
	v_add_u32_e32 v15, s57, v11
	v_lshlrev_b32_e32 v6, 12, v11
	v_bitop3_b32 v11, v15, v13, 15 bitop3:0x6c
	v_lshlrev_b32_e32 v11, 4, v11
	s_cselect_b32 s6, s76, s77
	v_lshl_or_b32 v13, v15, 12, v11
	v_add_u32_e32 v15, s58, v4
	s_or_b32 s44, s6, 0x80
	v_lshlrev_b32_e32 v16, 1, v15
	s_add_u32 s2, s71, s44
	v_and_b32_e32 v16, 0xffff0, v16
	v_and_b32_e32 v17, 4, v15
	s_addc_u32 s3, s70, 0
	v_or3_b32 v14, v17, v16, v14
	v_lshlrev_b32_e32 v15, 6, v15
	s_lshl_b64 s[36:37], s[2:3], 12
	v_and_b32_e32 v145, 31, v146
	v_and_b32_e32 v15, 0xc0, v15
	v_lshlrev_b32_e32 v14, 12, v14
	s_add_u32 s2, s79, s36
	v_or3_b32 v20, v14, v15, v3
	v_or_b32_e32 v14, s8, v145
	s_addc_u32 s3, s81, s37
	v_ashrrev_i32_e32 v15, 31, v14
	s_add_i32 s7, s6, 0x17f
	v_lshlrev_b64 v[14:15], 12, v[14:15]
	v_lshlrev_b32_e32 v16, 3, v4
	s_and_b32 s38, s7, 0x1f40
	v_lshl_add_u64 v[14:15], s[2:3], 0, v[14:15]
	v_ashrrev_i32_e32 v17, 31, v16
	s_lshl_b32 s33, s38, 12
	v_lshl_add_u64 v[14:15], v[16:17], 1, v[14:15]
	s_add_u32 s2, s82, s33
	global_load_dwordx4 v[112:115], v[14:15], off
	global_load_dwordx4 v[116:119], v[14:15], off offset:32
	global_load_dwordx4 v[120:123], v[14:15], off offset:64
	global_load_dwordx4 v[124:127], v[14:15], off offset:96
	global_load_dwordx4 v[128:131], v[14:15], off offset:128
	global_load_dwordx4 v[132:135], v[14:15], off offset:160
	global_load_dwordx4 v[136:139], v[14:15], off offset:192
	global_load_dwordx4 v[140:143], v[14:15], off offset:224
	s_addc_u32 s3, s83, 0
	s_add_u32 s34, s84, s33
	v_add_u32_e32 v0, s55, v6
	s_addc_u32 s35, s85, 0
	s_add_i32 s33, s68, 0x8000
	v_or_b32_e32 v18, v10, v0
	s_mov_b32 m0, s33
	v_add_u32_e32 v14, s38, v146
	global_load_lds_dwordx4 v18, s[2:3]
	s_mov_b32 m0, s68
	s_add_i32 s42, s68, 0x8400
	v_ashrrev_i32_e32 v15, 31, v14
	global_load_lds_dwordx4 v19, s[34:35]
	s_mov_b32 m0, s42
	s_add_i32 s43, s68, 0x400
	v_lshl_add_u64 v[14:15], v[14:15], 2, s[30:31]
	global_load_lds_dwordx4 v13, s[2:3]
	s_mov_b32 m0, s43
	global_load_dword v172, v[14:15], off
	v_cmp_ne_u32_e64 s[2:3], 1, v158
	global_load_lds_dwordx4 v20, s[34:35]
	s_lshr_b32 s100, s68, 11
	s_and_b32 s101, s100, 3
	s_lshl_b32 s98, s101, 12
	s_lshl_b32 s101, s101, 16
	s_lshr_b32 s45, s7, 6
	s_add_i32 s45, s45, -1
	s_lshl_b32 s47, s45, 8
	s_add_u32 s42, s30, s47
	s_addc_u32 s43, s31, 0
	s_lshl_b32 s47, s45, 18
	s_add_u32 s47, s47, s101
	v_lshlrev_b32_e32 v232, 2, v146
	s_cmp_ge_u32 s100, 4
	s_cbranch_scc1 .Lat_hb
	s_add_u32 s40, s82, s47
	s_addc_u32 s41, s83, 0
	v_lshrrev_b32_e32 v16, 4, v146
	v_and_b32_e32 v17, 15, v146
	v_xor_b32_e32 v17, v17, v16
	v_lshlrev_b32_e32 v17, 4, v17
	v_lshl_add_u32 v228, v16, 12, v17
	v_xor_b32_e32 v229, 0x40, v228
	v_add_u32_e32 v229, 0x4000, v229
	v_xor_b32_e32 v230, 0x80, v228
	v_add_u32_e32 v230, 0x8000, v230
	v_xor_b32_e32 v231, 0xc0, v228
	v_add_u32_e32 v231, 0xc000, v231
	s_add_i32 s65, s98, 0x11000
	s_mov_b32 s47, s65
	s_mov_b32 m0, s47
	s_add_i32 s47, s47, 0x400
	global_load_lds_dwordx4 v228, s[40:41]
	s_mov_b32 m0, s47
	s_add_i32 s47, s47, 0x400
	global_load_lds_dwordx4 v229, s[40:41]
	s_mov_b32 m0, s47
	s_add_i32 s47, s47, 0x400
	global_load_lds_dwordx4 v230, s[40:41]
	s_mov_b32 m0, s47
	s_nop 0
	global_load_lds_dwordx4 v231, s[40:41]
	global_load_dword v246, v232, s[42:43]
	s_sub_u32 s40, s40, 0x40000
	s_subb_u32 s41, s41, 0
	s_sub_u32 s42, s42, 0x100
	s_subb_u32 s43, s43, 0
	s_add_i32 s65, s98, 0x15000
	s_mov_b32 s47, s65
	s_mov_b32 m0, s47
	s_add_i32 s47, s47, 0x400
	global_load_lds_dwordx4 v228, s[40:41]
	s_mov_b32 m0, s47
	s_add_i32 s47, s47, 0x400
	global_load_lds_dwordx4 v229, s[40:41]
	s_mov_b32 m0, s47
	s_add_i32 s47, s47, 0x400
	global_load_lds_dwordx4 v230, s[40:41]
	s_mov_b32 m0, s47
	s_nop 0
	global_load_lds_dwordx4 v231, s[40:41]
	global_load_dword v247, v232, s[42:43]
	s_sub_u32 s40, s40, 0x40000
	s_subb_u32 s41, s41, 0
	s_sub_u32 s42, s42, 0x100
	s_subb_u32 s43, s43, 0
	s_add_i32 s65, s98, 0x19000
	s_mov_b32 s47, s65
	s_mov_b32 m0, s47
	s_add_i32 s47, s47, 0x400
	global_load_lds_dwordx4 v228, s[40:41]
	s_mov_b32 m0, s47
	s_add_i32 s47, s47, 0x400
	global_load_lds_dwordx4 v229, s[40:41]
	s_mov_b32 m0, s47
	s_add_i32 s47, s47, 0x400
	global_load_lds_dwordx4 v230, s[40:41]
	s_mov_b32 m0, s47
	s_nop 0
	global_load_lds_dwordx4 v231, s[40:41]
	global_load_dword v248, v232, s[42:43]
	s_sub_u32 s40, s40, 0x40000
	s_subb_u32 s41, s41, 0
	s_sub_u32 s42, s42, 0x100
	s_subb_u32 s43, s43, 0
	s_branch .Lat_hdone
.Lat_hb:
	s_add_u32 s40, s84, s47
	s_addc_u32 s41, s85, 0
	v_bfe_u32 v16, v146, 4, 1
	v_bfe_u32 v17, v146, 2, 2
	v_lshl_add_u32 v16, v16, 3, v17
	v_lshlrev_b32_e32 v16, 12, v16
	v_lshrrev_b32_e32 v17, 5, v146
	v_lshl_add_u32 v16, v17, 6, v16
	v_and_b32_e32 v17, 3, v146
	v_lshl_add_u32 v228, v17, 4, v16
	v_add_u32_e32 v229, 0x80, v228
	v_add_u32_e32 v230, 0x4000, v228
	v_add_u32_e32 v231, 0x4080, v228
	s_add_i32 s65, s98, 0x4000
	s_mov_b32 s47, s65
	s_mov_b32 m0, s47
	s_add_i32 s47, s47, 0x400
	global_load_lds_dwordx4 v228, s[40:41]
	s_mov_b32 m0, s47
	s_add_i32 s47, s47, 0x400
	global_load_lds_dwordx4 v229, s[40:41]
	s_mov_b32 m0, s47
	s_add_i32 s47, s47, 0x400
	global_load_lds_dwordx4 v230, s[40:41]
	s_mov_b32 m0, s47
	s_nop 0
	global_load_lds_dwordx4 v231, s[40:41]
.Lat_hdone:
	s_andn2_b64 vcc, exec, s[10:11]
	s_cbranch_vccnz .LBB0_1088
	v_lshl_add_u32 v13, v146, 2, 0
	v_add_u32_e32 v13, 0x10800, v13
	s_waitcnt vmcnt(0)
	ds_write_b32 v13, v172
.LBB0_1088:
	v_lshlrev_b32_e32 v13, 3, v146
	v_and_b32_e32 v12, 0xc0, v12
	v_lshlrev_b32_e32 v14, 1, v146
	s_xor_b64 s[34:35], s[4:5], -1
	v_and_or_b32 v12, v13, 24, v12
	v_and_b32_e32 v14, 32, v14
	v_and_b32_e32 v13, 0x100, v13
	s_add_i32 s44, s44, s8
	v_or3_b32 v12, v12, v14, v13
	v_or_b32_e32 v13, s44, v145
	s_cmp_lg_u32 0, -1
	s_cselect_b32 s4, 0, 0
	s_lshr_b32 s46, s7, 6
	v_add_u32_e32 v163, 0xffffff91, v13
	v_lshlrev_b32_e32 v164, 4, v4
	v_lshlrev_b32_e32 v13, 4, v145
	s_add_i32 s38, 0, 0x10800
	s_add_i32 s47, s46, -2
	s_or_b32 s64, s44, 31
	v_and_b32_e32 v13, 0x70, v13
	v_add_u32_e32 v14, 32, v164
	v_lshl_add_u32 v171, v146, 2, s38
	s_lshl_b32 s38, s46, 8
	v_xad_u32 v168, v14, v13, 0
	v_add_u32_e32 v14, 64, v164
	s_add_u32 s38, s89, s38
	v_xad_u32 v169, v14, v13, 0
	v_add_u32_e32 v14, 0x60, v164
	s_addc_u32 s39, s88, 0
	s_and_b32 s7, s7, 0x1fc0
	s_add_i32 s6, s60, s6
	v_lshlrev_b32_e32 v144, 2, v4
	v_xad_u32 v166, v13, v164, 0
	v_xad_u32 v170, v14, v13, 0
	s_sub_i32 s65, s7, 64
	v_add_u32_e32 v13, s6, v145
	s_lshl_b32 s6, s46, 18
	v_ashrrev_i32_e32 v147, 31, v146
	v_sub_u32_e32 v13, v13, v144
	s_add_u32 s6, s90, s6
	v_lshl_add_u64 v[148:149], v[146:147], 2, s[38:39]
	v_subrev_u32_e32 v147, s7, v13
	s_addc_u32 s7, s91, 0
	v_add_u32_e32 v0, v0, v10
	v_lshl_add_u64 v[150:151], s[6:7], 0, v[0:1]
	v_add3_u32 v0, s61, v6, v11
	v_lshl_add_u64 v[152:153], s[6:7], 0, v[0:1]
	v_add_u32_e32 v0, v7, v5
	v_add3_u32 v0, v0, v8, v2
	v_lshl_or_b32 v0, v0, 12, v9
	v_add_u32_e32 v0, v0, v3
	v_lshl_add_u64 v[154:155], s[6:7], 0, v[0:1]
	v_add_u32_e32 v0, s62, v4
	v_lshlrev_b32_e32 v4, 1, v0
	s_mov_b32 s38, 0xffff0
	v_and_or_b32 v4, v4, s38, v5
	v_and_b32_e32 v0, 4, v0
	v_add_u32_e32 v162, s4, v12
	v_lshrrev_b32_e32 v12, 5, v146
	v_add_u32_e32 v0, v4, v0
	v_add_lshl_u32 v0, v0, v2, 12
	v_add_u16_e32 v2, 2, v12
	v_and_b32_e32 v2, 3, v2
	v_lshlrev_b32_e32 v2, 6, v2
	s_waitcnt vmcnt(0)
	v_or3_b32 v0, v0, v2, v3
	v_mov_b32_e32 v14, v1
	v_mov_b32_e32 v15, v1
	v_lshl_add_u64 v[156:157], s[6:7], 0, v[0:1]
	v_mov_b32_e32 v0, v1
	v_mov_b32_e32 v2, v1
	v_mov_b32_e32 v3, v1
	v_mov_b32_e32 v4, v1
	v_mov_b32_e32 v5, v1
	v_mov_b32_e32 v6, v1
	v_mov_b32_e32 v7, v1
	v_mov_b32_e32 v8, v1
	v_mov_b32_e32 v9, v1
	v_mov_b32_e32 v10, v1
	v_mov_b32_e32 v11, v1
	v_mov_b32_e32 v12, v1
	v_mov_b32_e32 v13, v1
	s_waitcnt lgkmcnt(0)
	v_mov_b64_e32 v[30:31], v[14:15]
	v_mov_b64_e32 v[46:47], v[14:15]
	v_mov_b64_e32 v[62:63], v[14:15]
	v_mov_b64_e32 v[78:79], v[14:15]
	s_mov_b32 s45, 0
	v_lshlrev_b32_e32 v165, 8, v145
	v_cmp_gt_u32_e64 s[4:5], 32, v146
	v_lshl_add_u32 v167, v145, 2, s54
	v_add_u32_e32 v161, s54, v164
	v_mov_b32_e32 v174, 0
	v_mov_b32_e32 v173, 0xf149f2ca
	s_mov_b32 s66, s46
	v_mov_b64_e32 v[28:29], v[12:13]
	v_mov_b64_e32 v[26:27], v[10:11]
	v_mov_b64_e32 v[24:25], v[8:9]
	v_mov_b64_e32 v[22:23], v[6:7]
	v_mov_b64_e32 v[20:21], v[4:5]
	v_mov_b64_e32 v[18:19], v[2:3]
	v_mov_b64_e32 v[16:17], v[0:1]
	v_mov_b64_e32 v[44:45], v[12:13]
	v_mov_b64_e32 v[42:43], v[10:11]
	v_mov_b64_e32 v[40:41], v[8:9]
	v_mov_b64_e32 v[38:39], v[6:7]
	v_mov_b64_e32 v[36:37], v[4:5]
	v_mov_b64_e32 v[34:35], v[2:3]
	v_mov_b64_e32 v[32:33], v[0:1]
	v_mov_b64_e32 v[60:61], v[12:13]
	v_mov_b64_e32 v[58:59], v[10:11]
	v_mov_b64_e32 v[56:57], v[8:9]
	v_mov_b64_e32 v[54:55], v[6:7]
	v_mov_b64_e32 v[52:53], v[4:5]
	v_mov_b64_e32 v[50:51], v[2:3]
	v_mov_b64_e32 v[48:49], v[0:1]
	v_mov_b64_e32 v[76:77], v[12:13]
	v_mov_b64_e32 v[74:75], v[10:11]
	v_mov_b64_e32 v[72:73], v[8:9]
	v_mov_b64_e32 v[70:71], v[6:7]
	v_mov_b64_e32 v[68:69], v[4:5]
	v_mov_b64_e32 v[66:67], v[2:3]
	v_mov_b64_e32 v[64:65], v[0:1]
	s_waitcnt vmcnt(0)
	s_barrier
	s_mov_b32 s45, 0
	s_lshl_b32 s65, s46, 6
	s_mov_b32 s66, 0
	s_mov_b32 s33, 0x8000
	s_mov_b32 s42, 0x11000
	s_mov_b32 s43, 0x15000
	s_mov_b32 s47, 0x19000
	s_mov_b32 s99, 0
	v_subrev_u32_e32 v147, 64, v147
	v_lshlrev_b32_e32 v232, 2, v146
	s_lshr_b32 s6, s68, 11
	s_and_b32 s7, s6, 3
	s_lshl_b32 s98, s7, 12
	s_lshl_b32 s7, s7, 16
	s_add_i32 s40, s46, -1
	s_lshl_b32 s41, s40, 8
	s_lshl_b32 s39, s40, 18
	s_add_u32 s40, s30, s41
	s_addc_u32 s41, s31, 0
	s_add_u32 s39, s39, s7
	v_and_b32_e32 v0, 15, v145
	v_lshlrev_b32_e32 v0, 4, v0
	v_xor_b32_e32 v0, v0, v164
	v_xad_u32 v166, v0, 0, v165
	v_xad_u32 v168, v0, 32, v165
	v_xad_u32 v169, v0, 64, v165
	s_movk_i32 s7, 0x60
	v_xad_u32 v170, v0, s7, v165
	s_movk_i32 s7, 0x80
	v_xad_u32 v251, v0, s7, v165
	s_movk_i32 s7, 0xa0
	v_xad_u32 v252, v0, s7, v165
	s_movk_i32 s7, 0xc0
	v_xad_u32 v253, v0, s7, v165
	s_movk_i32 s7, 0xe0
	v_xad_u32 v254, v0, s7, v165
	s_cmp_ge_u32 s6, 4
	s_cbranch_scc1 .Lat_setup_b
	s_add_u32 s38, s82, s39
	s_addc_u32 s39, s83, 0
	s_sub_u32 s38, s38, 0xc0000
	s_subb_u32 s39, s39, 0
	s_sub_u32 s40, s40, 0x300
	s_subb_u32 s41, s41, 0
	s_waitcnt vmcnt(0)
	v_mov_b32_e32 v156, v248
	s_and_b64 vcc, exec, s[2:3]
	s_cbranch_vccnz .Lat_setup_done
	v_add_u32_e32 v0, 256, v171
	ds_write_b32 v0, v246
	v_add_u32_e32 v0, 512, v171
	ds_write_b32 v0, v247
	v_add_u32_e32 v0, 768, v171
	ds_write_b32 v0, v248
	s_waitcnt lgkmcnt(0)
	s_branch .Lat_setup_done
.Lat_setup_b:
	s_add_u32 s38, s84, s39
	s_addc_u32 s39, s85, 0
	s_sub_u32 s38, s38, 0x40000
	s_subb_u32 s39, s39, 0
